# v34
# baseline (speedup 1.0000x reference)
.LBB0_5:
	v_mad_legacy_u16 v2, v6, s8, v4
	v_lshlrev_b16_e32 v8, 15, v2
	v_lshrrev_b16_e32 v2, 1, v2
	v_cmp_lt_u32_e32 vcc, s24, v6
	v_or_b32_e32 v2, v2, v8
	s_or_b64 s[0:1], vcc, s[0:1]
	v_cmp_gt_u16_e32 vcc, s9, v2
	v_add_u32_e32 v7, 0x200, v6
	v_mov_b32_e32 v6, v7
	v_cndmask_b32_e32 v2, 0, v5, vcc
	ds_write_b64 v1, v[2:3]
	v_add_u32_e32 v1, 0x1000, v1
	s_andn2_b64 exec, exec, s[0:1]
	s_cbranch_execnz .LBB0_5
	s_or_b64 exec, exec, s[0:1]
	s_mov_b32 s34, 0
	v_cmp_eq_u32_e64 s[0:1], 0, v0
	s_and_saveexec_b64 s[8:9], s[0:1]
	v_mov_b32_e32 v1, 8
	v_mov_b32_e32 v2, 0x23420
	ds_write_b32 v2, v1
	s_or_b64 exec, exec, s[8:9]
	v_lshlrev_b32_e32 v1, 2, v131
	v_or_b32_e32 v2, 0x22200, v1
	v_or_b32_e32 v3, 0x22300, v1
	s_waitcnt lgkmcnt(0)
	s_barrier
	ds_read_b32 v2, v2
	ds_read_b32 v3, v3
	v_and_b32_e32 v202, 15, v0
	s_lshl_b32 s30, s31, 4
	v_or_b32_e32 v132, s30, v202
	s_waitcnt lgkmcnt(0)
	v_add_f32_e32 v2, v2, v3
	v_mbcnt_lo_u32_b32 v3, -1, 0
	v_mbcnt_hi_u32_b32 v3, -1, v3
	v_and_b32_e32 v4, 64, v3
	v_add_u32_e32 v4, 64, v4
	v_xor_b32_e32 v5, 32, v3
	v_cmp_lt_i32_e32 vcc, v5, v4
	v_mov_b32_e32 v133, 0
	v_lshrrev_b32_e32 v209, 4, v131
	v_cndmask_b32_e32 v5, v3, v5, vcc
	v_lshlrev_b32_e32 v200, 2, v5
	v_mov_b32_e32 v100, v133
	v_mov_b32_e32 v101, v133
	v_and_b32_e32 v203, 48, v0
	v_mov_b32_e32 v98, v133
	v_xor_b32_e32 v5, 16, v3
	v_cmp_lt_i32_e32 vcc, v5, v4
	v_mov_b32_e32 v99, v133
	v_mov_b64_e32 v[104:105], v[100:101]
	v_cndmask_b32_e32 v5, v3, v5, vcc
	v_lshlrev_b32_e32 v201, 2, v5
	v_mov_b64_e32 v[108:109], v[100:101]
	v_mov_b64_e32 v[112:113], v[100:101]
	v_mov_b64_e32 v[116:117], v[100:101]
	v_mov_b64_e32 v[120:121], v[100:101]
	v_xor_b32_e32 v5, 8, v3
	v_cmp_lt_i32_e32 vcc, v5, v4
	v_mov_b64_e32 v[124:125], v[100:101]
	v_mov_b64_e32 v[128:129], v[100:101]
	v_cndmask_b32_e32 v5, v3, v5, vcc
	v_lshlrev_b32_e32 v205, 2, v5
	v_cmp_eq_u32_e64 s[8:9], 0, v131
	v_mov_b32_e32 v218, 0xff800000
	v_mov_b32_e32 v213, 0x23420
	v_mov_b64_e32 v[102:103], v[98:99]
	v_xor_b32_e32 v5, 4, v3
	v_cmp_lt_i32_e32 vcc, v5, v4
	v_mov_b64_e32 v[106:107], v[98:99]
	v_mov_b64_e32 v[110:111], v[98:99]
	v_cndmask_b32_e32 v5, v3, v5, vcc
	v_lshlrev_b32_e32 v206, 2, v5
	v_mov_b64_e32 v[114:115], v[98:99]
	v_mov_b64_e32 v[118:119], v[98:99]
	v_mov_b64_e32 v[122:123], v[98:99]
	v_mov_b64_e32 v[126:127], v[98:99]
	v_xor_b32_e32 v5, 2, v3
	v_cmp_lt_i32_e32 vcc, v5, v4
	v_mov_b32_e32 v219, 0
	s_mov_b32 s35, s31
	v_cndmask_b32_e32 v5, v3, v5, vcc
	v_lshlrev_b32_e32 v207, 2, v5
	v_mov_b32_e32 v138, 0
	v_mov_b32_e32 v139, v133
	v_mov_b32_e32 v136, 0
	v_mov_b32_e32 v137, v133
	v_xor_b32_e32 v5, 1, v3
	v_cmp_lt_i32_e32 vcc, v5, v4
	v_lshlrev_b32_e32 v4, 3, v131
	v_mov_b32_e32 v144, 0
	v_cndmask_b32_e32 v3, v3, v5, vcc
	v_lshlrev_b32_e32 v208, 2, v3
	v_mov_b32_e32 v145, v133
	v_mov_b32_e32 v142, 0
	v_mov_b32_e32 v143, v133
	v_mov_b32_e32 v150, 0
	s_nop 1
	v_add_f32_dpp v2, v2, v2 row_shr:1 row_mask:0xf bank_mask:0xf
	s_nop 1
	v_add_f32_dpp v2, v2, v2 row_shr:2 row_mask:0xf bank_mask:0xf
	s_nop 1
	v_add_f32_dpp v2, v2, v2 row_shr:4 row_mask:0xf bank_mask:0xf
	s_nop 1
	v_add_f32_dpp v2, v2, v2 row_shr:8 row_mask:0xf bank_mask:0xf
	s_nop 1
	v_add_f32_dpp v2, v2, v2 row_bcast:15 row_mask:0xa bank_mask:0xf
	s_nop 1
	v_add_f32_dpp v2, v2, v2 row_bcast:31 row_mask:0xc bank_mask:0xf
	s_nop 1
	v_readlane_b32 s44, v2, 63
	s_nop 1
	v_mov_b32_e32 v2, s44
	v_add_f32_e32 v2, s43, v2
	s_mul_i32 s4, s31, 0x2200
	s_add_i32 s24, s4, 0x11000
	v_mul_f32_e32 v210, 0x3fb8aa3b, v2
	s_movk_i32 s4, 0x220
	v_mov_b32_e32 v2, s24
	v_mad_u32_u24 v5, v202, s4, v2
	v_lshlrev_b64 v[2:3], 9, v[132:133]
	v_lshl_add_u64 v[2:3], s[6:7], 0, v[2:3]
	v_lshlrev_b32_e32 v132, 5, v209
	v_add_u32_e32 v212, s24, v4
	v_mad_u32_u24 v211, v202, s4, v203
	v_lshl_add_u64 v[134:135], v[2:3], 0, v[132:133]
	v_cmp_eq_u32_e64 s[6:7], 15, v202
	v_cmp_eq_u32_e64 s[4:5], 15, v131
	v_add_u32_e32 v214, v5, v203
	v_add_u32_e32 v215, 0x800, v212
	v_add_u32_e32 v216, 0x1000, v212
	v_add_u32_e32 v217, 0x1800, v212
	v_mov_b32_e32 v151, v133
	v_mov_b32_e32 v140, 0
	v_mov_b32_e32 v141, v133
	v_mov_b32_e32 v148, 0
	v_mov_b32_e32 v149, v133
	v_mov_b32_e32 v146, 0
	v_mov_b32_e32 v147, v133
	v_mov_b32_e32 v178, 0
	v_mov_b32_e32 v179, v133
	v_mov_b32_e32 v168, 0
	v_mov_b32_e32 v169, v133
	v_mov_b32_e32 v154, 0
	v_mov_b32_e32 v155, v133
	v_mov_b32_e32 v152, 0
	v_mov_b32_e32 v153, v133
	v_mov_b32_e32 v182, 0
	v_mov_b32_e32 v183, v133
	v_mov_b32_e32 v180, 0
	v_mov_b32_e32 v181, v133
	v_mov_b32_e32 v158, 0
	v_mov_b32_e32 v159, v133
	v_mov_b32_e32 v156, 0
	v_mov_b32_e32 v157, v133
	v_mov_b32_e32 v186, 0
	v_mov_b32_e32 v187, v133
	v_mov_b32_e32 v184, 0
	v_mov_b32_e32 v185, v133
	v_mov_b32_e32 v162, 0
	v_mov_b32_e32 v163, v133
	v_mov_b32_e32 v160, 0
	v_mov_b32_e32 v161, v133
	v_mov_b32_e32 v190, 0
	v_mov_b32_e32 v191, v133
	v_mov_b32_e32 v188, 0
	v_mov_b32_e32 v189, v133
	v_mov_b32_e32 v166, 0
	v_mov_b32_e32 v167, v133
	v_mov_b32_e32 v164, 0
	v_mov_b32_e32 v165, v133
	v_mov_b32_e32 v194, 0
	v_mov_b32_e32 v195, v133
	v_mov_b32_e32 v192, 0
	v_mov_b32_e32 v193, v133
	v_mov_b32_e32 v172, 0
	v_mov_b32_e32 v173, v133
	v_mov_b32_e32 v170, 0
	v_mov_b32_e32 v171, v133
	v_mov_b32_e32 v198, 0
	v_mov_b32_e32 v199, v133
	v_mov_b32_e32 v196, 0
	v_mov_b32_e32 v197, v133
	v_mov_b32_e32 v176, 0
	v_mov_b32_e32 v177, v133
	v_mov_b32_e32 v174, 0
	v_mov_b32_e32 v175, v133
	s_cmp_eq_u32 s2, 0
	s_cselect_b64 s[24:25], -1, 0
	s_and_b64 s[24:25], s[24:25], s[10:11]
	s_and_saveexec_b64 s[26:27], s[24:25]
	s_cbranch_execz .Lp1_noinit
	global_store_dword v[254:255], v253, off sc0 sc1

.LBB0_78:
	s_or_b64 exec, exec, s[4:5]
	s_waitcnt lgkmcnt(0)
	s_barrier
	s_and_saveexec_b64 s[4:5], s[10:11]
	s_cbranch_execz .LBB0_81
	v_mov_b32_e32 v1, 0x23440
	v_mov_b32_e32 v6, 0x23450
	ds_read_b128 v[2:5], v1
	ds_read_b128 v[6:9], v6
	v_mov_b32_e32 v1, 0x23460
	ds_read_b128 v[10:13], v1
	s_mov_b32 s3, 0x3fb8aa3b
	s_waitcnt lgkmcnt(2)
	v_add_f32_e32 v1, s6, v2
	v_mov_b32_e32 v2, 0x23470
	ds_read_b128 v[14:17], v2
	v_mov_b32_e32 v2, 0x23480
	s_waitcnt lgkmcnt(2)
	v_add_f32_e32 v1, v1, v6
	v_mov_b32_e32 v6, 0x23490
	ds_read_b128 v[18:21], v2
	ds_read_b128 v[22:25], v6
	v_mov_b32_e32 v2, 0x234a0
	v_mov_b32_e32 v6, 0x234b0
	ds_read_b128 v[26:29], v2
	ds_read_b128 v[30:33], v6
	v_add_f32_e32 v2, s6, v3
	v_add_f32_e32 v2, v2, v7
	s_waitcnt lgkmcnt(5)
	v_add_f32_e32 v2, v2, v11
	s_waitcnt lgkmcnt(4)
	v_add_f32_e32 v2, v2, v15
	s_waitcnt lgkmcnt(3)
	v_add_f32_e32 v2, v2, v19
	s_waitcnt lgkmcnt(2)
	v_add_f32_e32 v2, v2, v23
	s_waitcnt lgkmcnt(1)
	v_add_f32_e32 v2, v2, v27
	s_waitcnt lgkmcnt(0)
	v_add_f32_e32 v3, v2, v31
	v_add_f32_e32 v2, s6, v4
	v_add_f32_e32 v2, v2, v8
	v_add_f32_e32 v2, v2, v12
	v_add_f32_e32 v2, v2, v16
	v_add_f32_e32 v2, v2, v20
	v_add_f32_e32 v2, v2, v24
	v_add_f32_e32 v2, v2, v28
	v_add_f32_e32 v6, v2, v32
	v_add_f32_e32 v2, s6, v5
	v_add_f32_e32 v2, v2, v9
	v_add_f32_e32 v2, v2, v13
	v_add_f32_e32 v1, v1, v10
	v_add_f32_e32 v2, v2, v17
	v_add_f32_e32 v1, v1, v14
	v_add_f32_e32 v2, v2, v21
	v_add_f32_e32 v1, v1, v18
	v_add_f32_e32 v2, v2, v25
	v_add_f32_e32 v1, v1, v22
	v_add_f32_e32 v2, v2, v29
	v_add_f32_e32 v1, v1, v26
	v_add_f32_e32 v10, v2, v33
	v_add_f32_e32 v1, v1, v30
	v_max_f32_e32 v2, v6, v10
	v_max3_f32 v2, v1, v3, v2
	v_sub_f32_e32 v1, v1, v2
	v_mul_f32_e32 v4, 0x3fb8aa3b, v1
	v_fma_f32 v5, v1, s3, -v4
	v_rndne_f32_e32 v7, v4
	v_fmac_f32_e32 v5, 0x32a5705f, v1
	v_sub_f32_e32 v4, v4, v7
	v_add_f32_e32 v4, v4, v5
	v_exp_f32_e32 v4, v4
	v_cvt_i32_f32_e32 v5, v7
	v_sub_f32_e32 v3, v3, v2
	v_mul_f32_e32 v12, 0x3fb8aa3b, v3
	s_mov_b32 s4, 0xc2ce8ed0
	v_fma_f32 v13, v3, s3, -v12
	v_rndne_f32_e32 v14, v12
	v_add_u32_e32 v8, 0x22c00, v130
	v_ldexp_f32 v4, v4, v5
	v_cmp_ngt_f32_e32 vcc, s4, v1
	v_fmac_f32_e32 v13, 0x32a5705f, v3
	v_sub_f32_e32 v12, v12, v14
	v_cndmask_b32_e32 v9, 0, v4, vcc
	ds_read2st64_b32 v[4:5], v8 offset1:2
	v_add_f32_e32 v12, v12, v13
	v_exp_f32_e32 v12, v12
	v_cvt_i32_f32_e32 v13, v14
	s_mov_b32 s5, 0x42b17218
	v_mov_b32_e32 v11, 0x7f800000
	v_cmp_nlt_f32_e32 vcc, s5, v1
	v_sub_f32_e32 v6, v6, v2
	v_mov_b32_e32 v7, 0
	v_cndmask_b32_e32 v1, v11, v9, vcc
	v_mul_f32_e32 v9, 0x3fb8aa3b, v6
	s_waitcnt lgkmcnt(0)
	v_fma_f32 v14, v1, v4, 0
	v_ldexp_f32 v4, v12, v13
	v_fma_f32 v12, v6, s3, -v9
	v_rndne_f32_e32 v13, v9
	v_fmac_f32_e32 v12, 0x32a5705f, v6
	v_sub_f32_e32 v9, v9, v13
	v_cmp_ngt_f32_e32 vcc, s4, v3
	v_add_f32_e32 v9, v9, v12
	v_exp_f32_e32 v9, v9
	v_cndmask_b32_e32 v4, 0, v4, vcc
	v_cvt_i32_f32_e32 v12, v13
	v_cmp_nlt_f32_e32 vcc, s5, v3
	s_nop 1
	v_cndmask_b32_e32 v3, v11, v4, vcc
	v_fmac_f32_e32 v14, v3, v5
	v_sub_f32_e32 v5, v10, v2
	v_mul_f32_e32 v10, 0x3fb8aa3b, v5
	v_ldexp_f32 v4, v9, v12
	v_fma_f32 v12, v5, s3, -v10
	v_rndne_f32_e32 v13, v10
	v_fmac_f32_e32 v12, 0x32a5705f, v5
	v_sub_f32_e32 v10, v10, v13
	v_add_f32_e32 v10, v10, v12
	v_exp_f32_e32 v10, v10
	v_cvt_i32_f32_e32 v12, v13
	ds_read2st64_b32 v[8:9], v8 offset0:4 offset1:6
	v_cmp_ngt_f32_e32 vcc, s4, v6
	s_nop 1
	v_cndmask_b32_e32 v4, 0, v4, vcc
	v_cmp_nlt_f32_e32 vcc, s5, v6
	v_ldexp_f32 v6, v10, v12
	s_nop 0
	v_cndmask_b32_e32 v4, v11, v4, vcc
	v_cmp_ngt_f32_e32 vcc, s4, v5
	s_waitcnt lgkmcnt(0)
	v_fmac_f32_e32 v14, v4, v8
	v_cndmask_b32_e32 v6, 0, v6, vcc
	v_cmp_nlt_f32_e32 vcc, s5, v5
	s_nop 1
	v_cndmask_b32_e32 v5, v11, v6, vcc
	s_lshl_b32 s36, s2, 2
	v_and_b32_e32 v6, 0x7c, v0
	v_lshl_or_b32 v6, v6, 8, s36
	v_and_or_b32 v6, v0, 3, v6
	v_fmac_f32_e32 v14, v5, v9
	v_lshl_add_u64 v[6:7], v[6:7], 2, s[20:21]
	global_store_dword v[6:7], v14, off sc0 sc1
	s_and_b64 exec, exec, s[0:1]
	s_cbranch_execz .LBB0_81
	s_lshl_b32 s0, s2, 1
	s_mov_b32 s1, 0
	v_add_f32_e32 v0, v1, v3
	s_lshl_b64 s[0:1], s[0:1], 2
	v_add_f32_e32 v0, v0, v4
	s_add_u32 s0, s20, s0
	v_add_f32_e32 v3, v0, v5
	s_addc_u32 s1, s21, s1
	v_mov_b32_e32 v0, 0x20000
	global_store_dwordx2 v0, v[2:3], s[0:1] sc0 sc1
